# v73 stack + MoE gate/up epilogue: pairs of 8-byte stores merged into one 16-byte store per lane via v_permlane16_swap
# speedup vs baseline: 1.0068x; 1.0068x over previous
.LBB0_791:
	ds_read_b64_tr_b16 v[116:117], v213
	ds_read_b64_tr_b16 v[118:119], v216
	ds_read_b64_tr_b16 v[120:121], v214
	ds_read_b64_tr_b16 v[122:123], v215
	ds_read_b128 v[124:127], v178
	v_readlane_b32 s76, v253, 4
	ds_read_b64_tr_b16 v[128:129], v211
	ds_read_b64_tr_b16 v[130:131], v212
	ds_read_b128 v[148:151], v178 offset:2304
	s_and_b64 s[14:15], s[12:13], exec
	v_readlane_b32 s79, v253, 7
	v_readlane_b32 s81, v253, 9
	v_readlane_b32 s85, v253, 13
	v_readlane_b32 s87, v253, 15
	v_readlane_b32 s78, v253, 6
	v_readlane_b32 s80, v253, 8
	v_readlane_b32 s84, v253, 12
	v_readlane_b32 s86, v253, 14
	s_cselect_b32 s17, s79, s85
	s_cselect_b32 s19, s81, s87
	s_cselect_b32 s16, s78, s84
	s_cselect_b32 s18, s80, s86
	s_lshl_b64 s[14:15], s[8:9], 20
	v_mov_b32_e32 v132, s19
	ds_read_b64_tr_b16 v[152:153], v145
	ds_read_b64_tr_b16 v[154:155], v147
	v_mov_b32_e32 v145, s17
	s_and_b64 s[12:13], s[12:13], exec
	v_cndmask_b32_e64 v161, v132, v145, s[4:5]
	v_mov_b32_e32 v132, s18
	s_waitcnt lgkmcnt(3)
	v_mfma_f32_16x16x32_bf16 v[156:159], v[128:131], v[124:127], v[104:107]
	s_cselect_b32 s13, s15, 0
	s_cselect_b32 s12, s14, 0
	v_mov_b32_e32 v145, v133
	v_mov_b32_e32 v104, s16
	v_cndmask_b32_e64 v160, v132, v104, s[4:5]
	v_lshl_add_u64 v[104:105], v[160:161], 0, s[12:13]
	s_lshl_b32 s12, s45, 6
	s_ashr_i32 s13, s12, 31
	v_lshl_add_u64 v[106:107], v[104:105], 0, v[134:135]
	s_lshl_b64 s[12:13], s[12:13], 2
	v_lshl_add_u64 v[106:107], v[106:107], 0, s[12:13]
	v_lshl_add_u64 v[106:107], v[106:107], 0, v[144:145]
	v_mov_b32_e32 v147, v133
	v_lshl_add_u64 v[106:107], v[106:107], 0, v[146:147]
	v_add_co_u32_e32 v164, vcc, s25, v106
	ds_read_b128 v[160:163], v178 offset:4608
	s_nop 0
	v_addc_co_u32_e32 v165, vcc, 0, v107, vcc
	v_mfma_f32_16x16x32_bf16 v[112:115], v[116:119], v[124:127], v[112:115]
	s_waitcnt vmcnt(8)
	v_cvt_pk_bf16_f32 v12, v12, v13
	v_cvt_pk_bf16_f32 v13, v14, v15
	s_waitcnt vmcnt(7)
	v_cvt_pk_bf16_f32 v8, v8, v9
	v_mfma_f32_16x16x32_bf16 v[108:111], v[120:123], v[124:127], v[108:111]
	v_cvt_pk_bf16_f32 v9, v10, v11
	v_readlane_b32 s77, v253, 5
	v_readlane_b32 s82, v253, 10
	s_waitcnt lgkmcnt(1)
	v_mfma_f32_16x16x32_bf16 v[100:103], v[152:155], v[124:127], v[100:103]
	v_readlane_b32 s83, v253, 11
	v_readlane_b32 s88, v253, 16
	v_readlane_b32 s89, v253, 17
	v_mfma_f32_16x16x32_bf16 v[96:99], v[116:119], v[148:151], v[96:99]
	v_readlane_b32 s90, v253, 18
	v_readlane_b32 s91, v253, 19
	v_mfma_f32_16x16x32_bf16 v[92:95], v[120:123], v[148:151], v[92:95]
	v_mfma_f32_16x16x32_bf16 v[124:127], v[128:131], v[148:151], v[20:23]
	v_mfma_f32_16x16x32_bf16 v[148:151], v[152:155], v[148:151], v[16:19]
	s_nop 1
	global_load_dwordx4 v[20:23], v[106:107], off
	global_load_dwordx4 v[16:19], v[164:165], off
	v_add_co_u32_e32 v164, vcc, s26, v106
	ds_read_b128 v[212:215], v178 offset:6912
	s_nop 0
	v_addc_co_u32_e32 v165, vcc, 0, v107, vcc
	v_add_co_u32_e32 v106, vcc, s27, v106
	s_waitcnt lgkmcnt(1)
	v_mfma_f32_16x16x32_bf16 v[216:219], v[120:123], v[160:163], v[28:31]
	v_addc_co_u32_e32 v107, vcc, 0, v107, vcc
	v_mfma_f32_16x16x32_bf16 v[220:223], v[128:131], v[160:163], v[24:27]
	s_nop 0
	global_load_dwordx4 v[28:31], v[164:165], off
	s_nop 0
	global_load_dwordx4 v[24:27], v[106:107], off
	ds_read_b128 v[224:227], v178 offset:9216
	ds_write_b64 v210, v[12:13]
	v_mfma_f32_16x16x32_bf16 v[88:91], v[116:119], v[160:163], v[88:91]
	ds_write_b64 v209, v[8:9]
	v_mfma_f32_16x16x32_bf16 v[64:67], v[152:155], v[160:163], v[64:67]
	s_waitcnt lgkmcnt(3)
	v_mfma_f32_16x16x32_bf16 v[8:11], v[116:119], v[212:215], v[52:55]
	s_waitcnt vmcnt(9)
	v_cvt_pk_bf16_f32 v0, v0, v1
	v_cvt_pk_bf16_f32 v1, v2, v3
	v_cvt_pk_bf16_f32 v106, v4, v5
	v_mfma_f32_16x16x32_bf16 v[12:15], v[120:123], v[212:215], v[60:63]
	v_cvt_pk_bf16_f32 v107, v6, v7
	v_mfma_f32_16x16x32_bf16 v[52:55], v[128:131], v[212:215], v[68:71]
	v_mfma_f32_16x16x32_bf16 v[60:63], v[152:155], v[212:215], v[76:79]
	s_waitcnt lgkmcnt(2)
	v_mfma_f32_16x16x32_bf16 v[68:71], v[116:119], v[224:227], v[84:87]
	s_nop 0
	ds_read_b128 v[76:79], v178 offset:64
	s_nop 0
	ds_read_b128 v[84:87], v178 offset:2368
	ds_read_b128 v[116:119], v178 offset:4672
	ds_write_b64 v206, v[0:1]
	v_mfma_f32_16x16x32_bf16 v[80:83], v[120:123], v[224:227], v[80:83]
	ds_write_b64 v208, v[106:107]
	v_mfma_f32_16x16x32_bf16 v[4:7], v[128:131], v[224:227], v[72:75]
	v_mfma_f32_16x16x32_bf16 v[0:3], v[152:155], v[224:227], v[56:59]
	s_nop 2
	ds_read_b64_tr_b16 v[56:57], v205
	ds_read_b64_tr_b16 v[58:59], v207
	ds_read_b64_tr_b16 v[72:73], v203
	ds_read_b64_tr_b16 v[74:75], v204
	ds_read_b64_tr_b16 v[120:121], v200
	ds_read_b64_tr_b16 v[122:123], v201
	ds_read_b64_tr_b16 v[128:129], v198
	ds_read_b64_tr_b16 v[130:131], v199
	s_waitcnt lgkmcnt(6)
	v_mfma_f32_16x16x32_bf16 v[112:115], v[56:59], v[76:79], v[112:115]
	s_waitcnt lgkmcnt(2)
	v_mfma_f32_16x16x32_bf16 v[152:155], v[120:123], v[76:79], v[156:159]
	s_nop 2
	ds_read_b128 v[156:159], v178 offset:6976
	ds_read_b128 v[160:163], v178 offset:9280
	s_waitcnt vmcnt(8)
	ds_write_b128 v195, v[32:35] offset:46080
	s_waitcnt vmcnt(7)
	ds_write_b128 v195, v[36:39] offset:55296
	v_mfma_f32_16x16x32_bf16 v[106:109], v[72:75], v[76:79], v[108:111]
	s_waitcnt lgkmcnt(4)
	v_mfma_f32_16x16x32_bf16 v[76:79], v[128:131], v[76:79], v[100:103]
	v_mfma_f32_16x16x32_bf16 v[96:99], v[56:59], v[84:87], v[96:99]
	v_mfma_f32_16x16x32_bf16 v[92:95], v[72:75], v[84:87], v[92:95]
	v_mfma_f32_16x16x32_bf16 v[100:103], v[120:123], v[84:87], v[124:127]
	v_mfma_f32_16x16x32_bf16 v[84:87], v[128:131], v[84:87], v[148:151]
	v_mfma_f32_16x16x32_bf16 v[88:91], v[56:59], v[116:119], v[88:91]
	v_mfma_f32_16x16x32_bf16 v[124:127], v[72:75], v[116:119], v[216:219]
	v_mfma_f32_16x16x32_bf16 v[148:151], v[120:123], v[116:119], v[220:223]
	v_mfma_f32_16x16x32_bf16 v[64:67], v[128:131], v[116:119], v[64:67]
	s_waitcnt lgkmcnt(3)
	v_mfma_f32_16x16x32_bf16 v[116:119], v[56:59], v[156:159], v[8:11]
	s_waitcnt vmcnt(6)
	ds_write_b128 v195, v[44:47] offset:64512
	s_waitcnt vmcnt(5)
	ds_write_b128 v196, v[48:51]
	s_waitcnt vmcnt(4)
	ds_write_b128 v197, v[40:43]
	v_add_u32_e32 v8, s48, v174
	ds_read_b32 v132, v202
	v_mfma_f32_16x16x32_bf16 v[196:199], v[72:75], v[156:159], v[12:15]
	s_waitcnt lgkmcnt(0)
	v_lshl_add_u64 v[10:11], v[132:133], 1, s[92:93]
	s_nop 0
	v_add_u32_e32 v14, 48, v8
	ds_read2st64_b32 v[8:9], v14 offset0:20 offset1:28
	ds_read2st64_b32 v[14:15], v14 offset0:36 offset1:44
	v_mfma_f32_16x16x32_bf16 v[56:59], v[56:59], v[160:163], v[68:71]
	s_waitcnt lgkmcnt(1)
	v_mov_b32_e32 v132, v8
	v_lshl_add_u64 v[12:13], v[132:133], 1, s[92:93]
	v_mov_b32_e32 v132, v9
	v_lshl_add_u64 v[8:9], v[132:133], 1, s[92:93]
	s_waitcnt lgkmcnt(0)
	v_mov_b32_e32 v132, v14
	global_load_dwordx4 v[36:39], v[10:11], off
	global_load_dwordx4 v[32:35], v[12:13], off
	v_lshl_add_u64 v[10:11], v[132:133], 1, s[92:93]
	v_mov_b32_e32 v132, v15
	v_mfma_f32_16x16x32_bf16 v[68:71], v[72:75], v[160:163], v[80:83]
	global_load_dwordx4 v[44:47], v[8:9], off
	global_load_dwordx4 v[40:43], v[10:11], off
	v_mfma_f32_16x16x32_bf16 v[72:75], v[120:123], v[160:163], v[4:7]
	s_nop 2
	v_lshl_add_u64 v[4:5], v[132:133], 1, s[92:93]
	global_load_dwordx4 v[48:51], v[4:5], off
	v_mfma_f32_16x16x32_bf16 v[52:55], v[120:123], v[156:159], v[52:55]
	v_mfma_f32_16x16x32_bf16 v[60:63], v[128:131], v[156:159], v[60:63]
	v_mfma_f32_16x16x32_bf16 v[80:83], v[128:131], v[160:163], v[0:3]
	s_barrier
	ds_read_b64_tr_b16 v[120:121], v193
	ds_read_b64_tr_b16 v[122:123], v194
	ds_read_b128 v[0:3], v178 offset:46080
	ds_read_b64_tr_b16 v[128:129], v190
	ds_read_b64_tr_b16 v[130:131], v191
	ds_read_b64_tr_b16 v[110:111], v192
	ds_read_b128 v[4:7], v178 offset:48384
	ds_read_b128 v[156:159], v178 offset:55296
	s_waitcnt lgkmcnt(5)
	v_mfma_f32_16x16x32_bf16 v[160:163], v[120:123], v[0:3], v[112:115]
	s_nop 2
	ds_read_b64_tr_b16 v[112:113], v189
	ds_read_b64_tr_b16 v[190:191], v187
	ds_read_b64_tr_b16 v[192:193], v188
	s_waitcnt lgkmcnt(6)
	v_mfma_f32_16x16x32_bf16 v[106:109], v[128:131], v[0:3], v[106:109]
	ds_read_b128 v[200:203], v178 offset:50688
	s_waitcnt lgkmcnt(3)
	v_mfma_f32_16x16x32_bf16 v[152:155], v[110:113], v[0:3], v[152:155]
	s_waitcnt lgkmcnt(1)
	v_mfma_f32_16x16x32_bf16 v[76:79], v[190:193], v[0:3], v[76:79]
	v_lshl_add_u64 v[0:1], v[104:105], 0, v[136:137]
	v_lshl_add_u64 v[0:1], v[0:1], 0, s[12:13]
	v_lshl_add_u64 v[0:1], v[0:1], 0, v[144:145]
	v_lshl_add_u64 v[0:1], v[0:1], 0, v[146:147]
	v_add_co_u32_e32 v2, vcc, s25, v0
	v_mfma_f32_16x16x32_bf16 v[96:99], v[120:123], v[4:7], v[96:99]
	s_nop 0
	v_addc_co_u32_e32 v3, vcc, 0, v1, vcc
	global_load_dwordx4 v[12:15], v[0:1], off
	global_load_dwordx4 v[8:11], v[2:3], off
	v_add_co_u32_e32 v2, vcc, s26, v0
	v_mfma_f32_16x16x32_bf16 v[92:95], v[128:131], v[4:7], v[92:95]
	s_nop 0
	v_addc_co_u32_e32 v3, vcc, 0, v1, vcc
	v_add_co_u32_e32 v0, vcc, s27, v0
	v_mfma_f32_16x16x32_bf16 v[100:103], v[110:113], v[4:7], v[100:103]
	s_nop 0
	v_addc_co_u32_e32 v1, vcc, 0, v1, vcc
	ds_read_b128 v[204:207], v178 offset:52992
	v_mfma_f32_16x16x32_bf16 v[84:87], v[190:193], v[4:7], v[84:87]
	global_load_dwordx4 v[4:7], v[2:3], off
	s_nop 0
	global_load_dwordx4 v[0:3], v[0:1], off
	s_waitcnt lgkmcnt(1)
	v_mfma_f32_16x16x32_bf16 v[88:91], v[120:123], v[200:203], v[88:91]
	v_mfma_f32_16x16x32_bf16 v[148:151], v[110:113], v[200:203], v[148:151]
	v_mfma_f32_16x16x32_bf16 v[64:67], v[190:193], v[200:203], v[64:67]
	v_mfma_f32_16x16x32_bf16 v[208:211], v[128:131], v[200:203], v[124:127]
	s_waitcnt lgkmcnt(0)
	v_mfma_f32_16x16x32_bf16 v[200:203], v[120:123], v[204:207], v[116:119]
	v_mfma_f32_16x16x32_bf16 v[194:197], v[128:131], v[204:207], v[196:199]
	v_mfma_f32_16x16x32_bf16 v[52:55], v[110:113], v[204:207], v[52:55]
	v_mfma_f32_16x16x32_bf16 v[60:63], v[190:193], v[204:207], v[60:63]
	v_mfma_f32_16x16x32_bf16 v[204:207], v[128:131], v[156:159], v[68:71]
	v_mfma_f32_16x16x32_bf16 v[212:215], v[110:113], v[156:159], v[72:75]
	s_nop 1
	ds_read_b128 v[68:71], v178 offset:46144
	ds_read_b128 v[72:75], v178 offset:48448
	ds_read_b128 v[216:219], v178 offset:50752
	v_mfma_f32_16x16x32_bf16 v[56:59], v[120:123], v[156:159], v[56:59]
	v_mfma_f32_16x16x32_bf16 v[156:159], v[190:193], v[156:159], v[80:83]
	ds_read_b64_tr_b16 v[188:189], v185
	ds_read_b64_tr_b16 v[190:191], v186
	ds_read_b64_tr_b16 v[220:221], v183
	ds_read_b64_tr_b16 v[222:223], v184
	s_waitcnt lgkmcnt(2)
	v_mfma_f32_16x16x32_bf16 v[124:127], v[188:191], v[68:71], v[160:163]
	s_nop 2
	ds_read_b64_tr_b16 v[160:161], v181
	ds_read_b64_tr_b16 v[162:163], v182
	ds_read_b64_tr_b16 v[182:183], v179
	ds_read_b64_tr_b16 v[184:185], v180
	s_waitcnt lgkmcnt(4)
	v_mfma_f32_16x16x32_bf16 v[116:119], v[220:223], v[68:71], v[106:109]
	s_waitcnt lgkmcnt(2)
	v_mfma_f32_16x16x32_bf16 v[128:131], v[160:163], v[68:71], v[152:155]
	s_waitcnt lgkmcnt(0)
	v_mfma_f32_16x16x32_bf16 v[120:123], v[182:185], v[68:71], v[76:79]
	v_mfma_f32_16x16x32_bf16 v[104:107], v[220:223], v[72:75], v[92:95]
	v_mfma_f32_16x16x32_bf16 v[92:95], v[160:163], v[216:219], v[148:151]
	ds_read_b128 v[68:71], v178 offset:53056
	s_nop 1
	ds_read_b128 v[148:151], v178 offset:55360
	v_mfma_f32_16x16x32_bf16 v[112:115], v[188:191], v[72:75], v[96:99]
	v_mfma_f32_16x16x32_bf16 v[108:111], v[160:163], v[72:75], v[100:103]
	v_mfma_f32_16x16x32_bf16 v[100:103], v[182:185], v[72:75], v[84:87]
	v_mfma_f32_16x16x32_bf16 v[96:99], v[188:191], v[216:219], v[88:91]
	v_mfma_f32_16x16x32_bf16 v[84:87], v[220:223], v[216:219], v[208:211]
	v_mfma_f32_16x16x32_bf16 v[88:91], v[182:185], v[216:219], v[64:67]
	s_waitcnt lgkmcnt(1)
	v_mfma_f32_16x16x32_bf16 v[80:83], v[188:191], v[68:71], v[200:203]
	v_mfma_f32_16x16x32_bf16 v[72:75], v[220:223], v[68:71], v[194:197]
	v_mfma_f32_16x16x32_bf16 v[76:79], v[160:163], v[68:71], v[52:55]
	v_mfma_f32_16x16x32_bf16 v[68:71], v[182:185], v[68:71], v[60:63]
	s_waitcnt lgkmcnt(0)
	v_mfma_f32_16x16x32_bf16 v[64:67], v[188:191], v[148:151], v[56:59]
	v_mfma_f32_16x16x32_bf16 v[56:59], v[220:223], v[148:151], v[204:207]
	v_mfma_f32_16x16x32_bf16 v[60:63], v[160:163], v[148:151], v[212:215]
	v_mfma_f32_16x16x32_bf16 v[52:55], v[182:185], v[148:151], v[156:159]
	v_add_u32_e32 v145, s23, v169
	v_cmp_lt_i32_e32 vcc, v145, v166
	v_lshlrev_b32_e32 v132, 1, v138
	v_lshlrev_b32_e32 v148, 1, v140
	v_mbcnt_lo_u32_b32 v228, -1, 0
	v_mbcnt_hi_u32_b32 v228, -1, v228
	v_bfe_u32 v228, v228, 4, 1
	v_mul_u32_u24_e32 v228, 24, v228
	v_add_u32_e32 v148, v148, v228
	s_and_saveexec_b64 s[12:13], vcc
	s_cbranch_execz .LBB0_793
	v_mul_f32_e32 v147, 0xbfb8aa3b, v124
	v_exp_f32_e32 v147, v147
	v_readlane_b32 s14, v254, 1
	v_readlane_b32 s15, v254, 2
	v_mov_b32_e32 v149, v133
	v_add_f32_e32 v147, 1.0, v147
	v_rcp_f32_e32 v150, v147
	v_mul_f32_e32 v147, 0xbfb8aa3b, v125
	v_exp_f32_e32 v147, v147
	s_nop 0
	v_add_f32_e32 v147, 1.0, v147
	v_rcp_f32_e32 v151, v147
	s_nop 0
	v_pk_mul_f32 v[124:125], v[124:125], v[150:151]
	s_nop 0
	v_pk_mul_f32 v[124:125], v[128:129], v[124:125]
	v_mul_f32_e32 v128, 0xbfb8aa3b, v126
	v_mul_f32_e32 v129, 0xbfb8aa3b, v127
	v_exp_f32_e32 v128, v128
	v_exp_f32_e32 v129, v129
	v_cvt_pk_bf16_f32 v124, v124, v125
	v_add_f32_e32 v128, 1.0, v128
	v_add_f32_e32 v129, 1.0, v129
	v_rcp_f32_e32 v128, v128
	v_rcp_f32_e32 v129, v129
	s_nop 0
	v_pk_mul_f32 v[126:127], v[126:127], v[128:129]
	v_add_u32_e32 v128, v139, v145
	v_ashrrev_i32_e32 v129, 31, v128
	v_lshlrev_b64 v[128:129], 9, v[128:129]
	v_lshl_add_u64 v[128:129], s[14:15], 0, v[128:129]
	v_lshl_add_u64 v[128:129], s[10:11], 1, v[128:129]
	v_pk_mul_f32 v[126:127], v[130:131], v[126:127]
	v_lshl_add_u64 v[128:129], v[128:129], 0, v[132:133]
	v_lshl_add_u64 v[128:129], v[128:129], 0, v[148:149]
	v_cvt_pk_bf16_f32 v125, v126, v127
	v_mov_b32_e32 v224, v124
	v_mov_b32_e32 v225, v125
	v_mul_f32_e32 v124, 0xbfb8aa3b, v116
	v_mul_f32_e32 v125, 0xbfb8aa3b, v117
	v_exp_f32_e32 v124, v124
	v_exp_f32_e32 v125, v125
	v_add_f32_e32 v124, 1.0, v124
	v_add_f32_e32 v125, 1.0, v125
	v_rcp_f32_e32 v124, v124
	v_rcp_f32_e32 v125, v125
	s_nop 0
	v_pk_mul_f32 v[116:117], v[116:117], v[124:125]
	s_nop 0
	v_pk_mul_f32 v[116:117], v[120:121], v[116:117]
	v_mul_f32_e32 v120, 0xbfb8aa3b, v118
	v_mul_f32_e32 v121, 0xbfb8aa3b, v119
	v_exp_f32_e32 v120, v120
	v_exp_f32_e32 v121, v121
	v_cvt_pk_bf16_f32 v116, v116, v117
	v_add_f32_e32 v120, 1.0, v120
	v_add_f32_e32 v121, 1.0, v121
	v_rcp_f32_e32 v120, v120
	v_rcp_f32_e32 v121, v121
	s_nop 0
	v_pk_mul_f32 v[118:119], v[118:119], v[120:121]
	s_nop 0
	v_pk_mul_f32 v[118:119], v[122:123], v[118:119]
	s_nop 0
	v_cvt_pk_bf16_f32 v117, v118, v119
	v_mov_b32_e32 v226, v116
	v_mov_b32_e32 v227, v117
	s_nop 1
	v_permlane16_swap_b32 v224, v226
	v_permlane16_swap_b32 v225, v227
	global_store_dwordx4 v[128:129], v[224:227], off
.LBB0_793:
	s_or_b64 exec, exec, s[12:13]
	v_add_u32_e32 v116, s23, v252
	v_cmp_lt_i32_e32 vcc, v116, v166
	s_and_saveexec_b64 s[12:13], vcc
	s_cbranch_execz .LBB0_795
	v_mul_f32_e32 v117, 0xbfb8aa3b, v112
	v_exp_f32_e32 v117, v117
	v_readlane_b32 s14, v254, 1
	v_readlane_b32 s15, v254, 2
	v_mov_b32_e32 v149, v133
	v_add_f32_e32 v117, 1.0, v117
	v_rcp_f32_e32 v118, v117
	v_mul_f32_e32 v117, 0xbfb8aa3b, v113
	v_exp_f32_e32 v117, v117
	s_nop 0
	v_add_f32_e32 v117, 1.0, v117
	v_rcp_f32_e32 v119, v117
	s_nop 0
	v_pk_mul_f32 v[112:113], v[112:113], v[118:119]
	s_nop 0
	v_pk_mul_f32 v[108:109], v[108:109], v[112:113]
	v_mul_f32_e32 v112, 0xbfb8aa3b, v114
	v_mul_f32_e32 v113, 0xbfb8aa3b, v115
	v_exp_f32_e32 v112, v112
	v_exp_f32_e32 v113, v113
	v_cvt_pk_bf16_f32 v108, v108, v109
	v_add_f32_e32 v112, 1.0, v112
	v_add_f32_e32 v113, 1.0, v113
	v_rcp_f32_e32 v112, v112
	v_rcp_f32_e32 v113, v113
	s_nop 0
	v_pk_mul_f32 v[112:113], v[114:115], v[112:113]
	s_nop 0
	v_pk_mul_f32 v[110:111], v[110:111], v[112:113]
	v_add_u32_e32 v112, v139, v116
	v_ashrrev_i32_e32 v113, 31, v112
	v_lshlrev_b64 v[112:113], 9, v[112:113]
	v_lshl_add_u64 v[112:113], s[14:15], 0, v[112:113]
	v_lshl_add_u64 v[112:113], s[10:11], 1, v[112:113]
	v_lshl_add_u64 v[112:113], v[112:113], 0, v[132:133]
	v_lshl_add_u64 v[112:113], v[112:113], 0, v[148:149]
	v_cvt_pk_bf16_f32 v109, v110, v111
	v_mov_b32_e32 v224, v108
	v_mov_b32_e32 v225, v109
	v_mul_f32_e32 v108, 0xbfb8aa3b, v104
	v_mul_f32_e32 v109, 0xbfb8aa3b, v105
	v_exp_f32_e32 v108, v108
	v_exp_f32_e32 v109, v109
	v_add_f32_e32 v108, 1.0, v108
	v_add_f32_e32 v109, 1.0, v109
	v_rcp_f32_e32 v108, v108
	v_rcp_f32_e32 v109, v109
	s_nop 0
	v_pk_mul_f32 v[104:105], v[104:105], v[108:109]
	s_nop 0
	v_pk_mul_f32 v[100:101], v[100:101], v[104:105]
	v_mul_f32_e32 v104, 0xbfb8aa3b, v106
	v_mul_f32_e32 v105, 0xbfb8aa3b, v107
	v_exp_f32_e32 v104, v104
	v_exp_f32_e32 v105, v105
	v_cvt_pk_bf16_f32 v100, v100, v101
	v_add_f32_e32 v104, 1.0, v104
	v_add_f32_e32 v105, 1.0, v105
	v_rcp_f32_e32 v104, v104
	v_rcp_f32_e32 v105, v105
	s_nop 0
	v_pk_mul_f32 v[104:105], v[106:107], v[104:105]
	s_nop 0
	v_pk_mul_f32 v[102:103], v[102:103], v[104:105]
	s_nop 0
	v_cvt_pk_bf16_f32 v101, v102, v103
	v_mov_b32_e32 v226, v100
	v_mov_b32_e32 v227, v101
	s_nop 1
	v_permlane16_swap_b32 v224, v226
	v_permlane16_swap_b32 v225, v227
	global_store_dwordx4 v[112:113], v[224:227], off
.LBB0_795:
	s_or_b64 exec, exec, s[12:13]
	v_add_u32_e32 v100, 32, v169
	v_add_u32_e32 v100, s23, v100
	v_cmp_lt_i32_e32 vcc, v100, v166
	s_and_saveexec_b64 s[12:13], vcc
	s_cbranch_execz .LBB0_797
	v_mul_f32_e32 v101, 0xbfb8aa3b, v96
	v_exp_f32_e32 v101, v101
	v_readlane_b32 s14, v254, 1
	v_readlane_b32 s15, v254, 2
	v_mov_b32_e32 v149, v133
	v_add_f32_e32 v101, 1.0, v101
	v_rcp_f32_e32 v102, v101
	v_mul_f32_e32 v101, 0xbfb8aa3b, v97
	v_exp_f32_e32 v101, v101
	s_nop 0
	v_add_f32_e32 v101, 1.0, v101
	v_rcp_f32_e32 v103, v101
	s_nop 0
	v_pk_mul_f32 v[96:97], v[96:97], v[102:103]
	s_nop 0
	v_pk_mul_f32 v[92:93], v[92:93], v[96:97]
	v_mul_f32_e32 v96, 0xbfb8aa3b, v98
	v_mul_f32_e32 v97, 0xbfb8aa3b, v99
	v_exp_f32_e32 v96, v96
	v_exp_f32_e32 v97, v97
	v_cvt_pk_bf16_f32 v92, v92, v93
	v_add_f32_e32 v96, 1.0, v96
	v_add_f32_e32 v97, 1.0, v97
	v_rcp_f32_e32 v96, v96
	v_rcp_f32_e32 v97, v97
	s_nop 0
	v_pk_mul_f32 v[96:97], v[98:99], v[96:97]
	s_nop 0
	v_pk_mul_f32 v[94:95], v[94:95], v[96:97]
	v_add_u32_e32 v96, v139, v100
	v_ashrrev_i32_e32 v97, 31, v96
	v_lshlrev_b64 v[96:97], 9, v[96:97]
	v_lshl_add_u64 v[96:97], s[14:15], 0, v[96:97]
	v_lshl_add_u64 v[96:97], s[10:11], 1, v[96:97]
	v_lshl_add_u64 v[96:97], v[96:97], 0, v[132:133]
	v_lshl_add_u64 v[96:97], v[96:97], 0, v[148:149]
	v_cvt_pk_bf16_f32 v93, v94, v95
	v_mov_b32_e32 v224, v92
	v_mov_b32_e32 v225, v93
	v_mul_f32_e32 v92, 0xbfb8aa3b, v84
	v_mul_f32_e32 v93, 0xbfb8aa3b, v85
	v_exp_f32_e32 v92, v92
	v_exp_f32_e32 v93, v93
	v_add_f32_e32 v92, 1.0, v92
	v_add_f32_e32 v93, 1.0, v93
	v_rcp_f32_e32 v92, v92
	v_rcp_f32_e32 v93, v93
	s_nop 0
	v_pk_mul_f32 v[84:85], v[84:85], v[92:93]
	s_nop 0
	v_pk_mul_f32 v[84:85], v[88:89], v[84:85]
	v_mul_f32_e32 v88, 0xbfb8aa3b, v86
	v_mul_f32_e32 v89, 0xbfb8aa3b, v87
	v_exp_f32_e32 v88, v88
	v_exp_f32_e32 v89, v89
	v_cvt_pk_bf16_f32 v84, v84, v85
	v_add_f32_e32 v88, 1.0, v88
	v_add_f32_e32 v89, 1.0, v89
	v_rcp_f32_e32 v88, v88
	v_rcp_f32_e32 v89, v89
	s_nop 0
	v_pk_mul_f32 v[86:87], v[86:87], v[88:89]
	s_nop 0
	v_pk_mul_f32 v[86:87], v[90:91], v[86:87]
	s_nop 0
	v_cvt_pk_bf16_f32 v85, v86, v87
	v_mov_b32_e32 v226, v84
	v_mov_b32_e32 v227, v85
	s_nop 1
	v_permlane16_swap_b32 v224, v226
	v_permlane16_swap_b32 v225, v227
	global_store_dwordx4 v[96:97], v[224:227], off
.LBB0_797:
	s_or_b64 exec, exec, s[12:13]
	v_add_u32_e32 v84, 48, v169
	v_add_u32_e32 v84, s23, v84
	v_cmp_lt_i32_e32 vcc, v84, v166
	s_and_saveexec_b64 s[12:13], vcc
	s_cbranch_execz .LBB0_799
	v_mul_f32_e32 v85, 0xbfb8aa3b, v80
	v_exp_f32_e32 v85, v85
	v_readlane_b32 s14, v254, 1
	v_readlane_b32 s15, v254, 2
	v_mov_b32_e32 v149, v133
	v_add_f32_e32 v85, 1.0, v85
	v_rcp_f32_e32 v86, v85
	v_mul_f32_e32 v85, 0xbfb8aa3b, v81
	v_exp_f32_e32 v85, v85
	s_nop 0
	v_add_f32_e32 v85, 1.0, v85
	v_rcp_f32_e32 v87, v85
	s_nop 0
	v_pk_mul_f32 v[80:81], v[80:81], v[86:87]
	s_nop 0
	v_pk_mul_f32 v[76:77], v[76:77], v[80:81]
	v_mul_f32_e32 v80, 0xbfb8aa3b, v82
	v_mul_f32_e32 v81, 0xbfb8aa3b, v83
	v_exp_f32_e32 v80, v80
	v_exp_f32_e32 v81, v81
	v_cvt_pk_bf16_f32 v76, v76, v77
	v_add_f32_e32 v80, 1.0, v80
	v_add_f32_e32 v81, 1.0, v81
	v_rcp_f32_e32 v80, v80
	v_rcp_f32_e32 v81, v81
	s_nop 0
	v_pk_mul_f32 v[80:81], v[82:83], v[80:81]
	s_nop 0
	v_pk_mul_f32 v[78:79], v[78:79], v[80:81]
	v_add_u32_e32 v80, v139, v84
	v_ashrrev_i32_e32 v81, 31, v80
	v_lshlrev_b64 v[80:81], 9, v[80:81]
	v_lshl_add_u64 v[80:81], s[14:15], 0, v[80:81]
	v_lshl_add_u64 v[80:81], s[10:11], 1, v[80:81]
	v_lshl_add_u64 v[80:81], v[80:81], 0, v[132:133]
	v_lshl_add_u64 v[80:81], v[80:81], 0, v[148:149]
	v_cvt_pk_bf16_f32 v77, v78, v79
	v_mov_b32_e32 v224, v76
	v_mov_b32_e32 v225, v77
	v_mul_f32_e32 v76, 0xbfb8aa3b, v72
	v_mul_f32_e32 v77, 0xbfb8aa3b, v73
	v_exp_f32_e32 v76, v76
	v_exp_f32_e32 v77, v77
	v_add_f32_e32 v76, 1.0, v76
	v_add_f32_e32 v77, 1.0, v77
	v_rcp_f32_e32 v76, v76
	v_rcp_f32_e32 v77, v77
	s_nop 0
	v_pk_mul_f32 v[72:73], v[72:73], v[76:77]
	s_nop 0
	v_pk_mul_f32 v[68:69], v[68:69], v[72:73]
	v_mul_f32_e32 v72, 0xbfb8aa3b, v74
	v_mul_f32_e32 v73, 0xbfb8aa3b, v75
	v_exp_f32_e32 v72, v72
	v_exp_f32_e32 v73, v73
	v_cvt_pk_bf16_f32 v68, v68, v69
	v_add_f32_e32 v72, 1.0, v72
	v_add_f32_e32 v73, 1.0, v73
	v_rcp_f32_e32 v72, v72
	v_rcp_f32_e32 v73, v73
	s_nop 0
	v_pk_mul_f32 v[72:73], v[74:75], v[72:73]
	s_nop 0
	v_pk_mul_f32 v[70:71], v[70:71], v[72:73]
	s_nop 0
	v_cvt_pk_bf16_f32 v69, v70, v71
	v_mov_b32_e32 v226, v68
	v_mov_b32_e32 v227, v69
	s_nop 1
	v_permlane16_swap_b32 v224, v226
	v_permlane16_swap_b32 v225, v227
	global_store_dwordx4 v[80:81], v[224:227], off

.LBB0_801:
	v_mul_f32_e32 v69, 0xbfb8aa3b, v64
	v_exp_f32_e32 v69, v69
	v_readlane_b32 s14, v254, 1
	v_readlane_b32 s15, v254, 2
	v_mov_b32_e32 v149, v133
	v_add_f32_e32 v69, 1.0, v69
	v_rcp_f32_e32 v70, v69
	v_mul_f32_e32 v69, 0xbfb8aa3b, v65
	v_exp_f32_e32 v69, v69
	s_nop 0
	v_add_f32_e32 v69, 1.0, v69
	v_rcp_f32_e32 v71, v69
	s_nop 0
	v_pk_mul_f32 v[64:65], v[64:65], v[70:71]
	s_nop 0
	v_pk_mul_f32 v[60:61], v[60:61], v[64:65]
	v_mul_f32_e32 v64, 0xbfb8aa3b, v66
	v_mul_f32_e32 v65, 0xbfb8aa3b, v67
	v_exp_f32_e32 v64, v64
	v_exp_f32_e32 v65, v65
	v_cvt_pk_bf16_f32 v60, v60, v61
	v_add_f32_e32 v64, 1.0, v64
	v_add_f32_e32 v65, 1.0, v65
	v_rcp_f32_e32 v64, v64
	v_rcp_f32_e32 v65, v65
	s_nop 0
	v_pk_mul_f32 v[64:65], v[66:67], v[64:65]
	s_nop 0
	v_pk_mul_f32 v[62:63], v[62:63], v[64:65]
	v_add_u32_e32 v64, v139, v68
	v_ashrrev_i32_e32 v65, 31, v64
	v_lshlrev_b64 v[64:65], 9, v[64:65]
	v_lshl_add_u64 v[64:65], s[14:15], 0, v[64:65]
	v_lshl_add_u64 v[64:65], s[10:11], 1, v[64:65]
	v_lshl_add_u64 v[64:65], v[64:65], 0, v[132:133]
	v_lshl_add_u64 v[64:65], v[64:65], 0, v[148:149]
	v_cvt_pk_bf16_f32 v61, v62, v63
	v_mov_b32_e32 v224, v60
	v_mov_b32_e32 v225, v61
	v_mul_f32_e32 v60, 0xbfb8aa3b, v56
	v_mul_f32_e32 v61, 0xbfb8aa3b, v57
	v_exp_f32_e32 v60, v60
	v_exp_f32_e32 v61, v61
	v_add_f32_e32 v60, 1.0, v60
	v_add_f32_e32 v61, 1.0, v61
	v_rcp_f32_e32 v60, v60
	v_rcp_f32_e32 v61, v61
	s_nop 0
	v_pk_mul_f32 v[56:57], v[56:57], v[60:61]
	s_nop 0
	v_pk_mul_f32 v[52:53], v[52:53], v[56:57]
	v_mul_f32_e32 v56, 0xbfb8aa3b, v58
	v_mul_f32_e32 v57, 0xbfb8aa3b, v59
	v_exp_f32_e32 v56, v56
	v_exp_f32_e32 v57, v57
	v_cvt_pk_bf16_f32 v52, v52, v53
	v_add_f32_e32 v56, 1.0, v56
	v_add_f32_e32 v57, 1.0, v57
	v_rcp_f32_e32 v56, v56
	v_rcp_f32_e32 v57, v57
	s_nop 0
	v_pk_mul_f32 v[56:57], v[58:59], v[56:57]
	s_nop 0
	v_pk_mul_f32 v[54:55], v[54:55], v[56:57]
	s_nop 0
	v_cvt_pk_bf16_f32 v53, v54, v55
	v_mov_b32_e32 v226, v52
	v_mov_b32_e32 v227, v53
	s_nop 1
	v_permlane16_swap_b32 v224, v226
	v_permlane16_swap_b32 v225, v227
	global_store_dwordx4 v[64:65], v[224:227], off
	s_or_b64 exec, exec, s[12:13]
	v_cmp_ne_u32_e32 vcc, 1, v177
	s_cbranch_vccnz .LBB0_776

.LBB0_2371:
	v_readlane_b32 s76, v253, 4
	v_readlane_b32 s84, v253, 12
	v_readlane_b32 s85, v253, 13
	v_readlane_b32 s86, v253, 14
	v_readlane_b32 s87, v253, 15
	v_readlane_b32 s88, v253, 16
	v_readlane_b32 s89, v253, 17
	v_readlane_b32 s90, v253, 18
	v_readlane_b32 s91, v253, 19
	s_mov_b64 s[56:57], s[84:85]
	s_and_b64 s[16:17], s[14:15], exec
	s_mov_b64 s[58:59], s[86:87]
	s_cselect_b32 s19, s28, s57
	s_cselect_b32 s21, s33, s59
	s_cselect_b32 s18, s27, s56
	s_cselect_b32 s20, s29, s58
	s_lshl_b64 s[16:17], s[10:11], 20
	ds_read_b64_tr_b16 v[116:117], v213
	ds_read_b64_tr_b16 v[118:119], v216
	ds_read_b64_tr_b16 v[120:121], v214
	ds_read_b64_tr_b16 v[122:123], v215
	ds_read_b128 v[124:127], v178
	ds_read_b64_tr_b16 v[128:129], v211
	ds_read_b64_tr_b16 v[130:131], v212
	ds_read_b128 v[148:151], v178 offset:2304
	v_mov_b32_e32 v132, s21
	ds_read_b64_tr_b16 v[152:153], v145
	ds_read_b64_tr_b16 v[154:155], v147
	v_mov_b32_e32 v145, s19
	s_and_b64 s[14:15], s[14:15], exec
	v_cndmask_b32_e64 v157, v132, v145, s[4:5]
	v_mov_b32_e32 v132, s20
	v_mov_b32_e32 v145, s18
	s_cselect_b32 s15, s17, 0
	s_cselect_b32 s14, s16, 0x100000
	v_cndmask_b32_e64 v156, v132, v145, s[4:5]
	v_lshl_add_u64 v[164:165], v[156:157], 0, s[14:15]
	s_lshl_b32 s14, s48, 6
	s_ashr_i32 s15, s14, 31
	s_waitcnt lgkmcnt(5)
	v_mfma_f32_16x16x32_bf16 v[112:115], v[116:119], v[124:127], v[112:115]
	s_lshl_b64 s[14:15], s[14:15], 2
	v_mov_b32_e32 v145, v133
	v_mov_b32_e32 v147, v133
	v_mfma_f32_16x16x32_bf16 v[108:111], v[120:123], v[124:127], v[108:111]
	ds_read_b128 v[156:159], v178 offset:4608
	s_waitcnt vmcnt(8)
	v_cvt_pk_bf16_f32 v12, v12, v13
	v_cvt_pk_bf16_f32 v13, v14, v15
	s_waitcnt lgkmcnt(4)
	v_mfma_f32_16x16x32_bf16 v[104:107], v[128:131], v[124:127], v[104:107]
	s_waitcnt vmcnt(7)
	v_cvt_pk_bf16_f32 v8, v8, v9
	v_cvt_pk_bf16_f32 v9, v10, v11
	v_readlane_b32 s77, v253, 5
	s_waitcnt lgkmcnt(1)
	v_mfma_f32_16x16x32_bf16 v[100:103], v[152:155], v[124:127], v[100:103]
	v_lshl_add_u64 v[124:125], v[164:165], 0, v[134:135]
	v_lshl_add_u64 v[124:125], v[124:125], 0, s[14:15]
	v_lshl_add_u64 v[124:125], v[124:125], 0, v[144:145]
	v_lshl_add_u64 v[170:171], v[124:125], 0, v[146:147]
	v_add_co_u32_e32 v160, vcc, s34, v170
	v_mfma_f32_16x16x32_bf16 v[96:99], v[116:119], v[148:151], v[96:99]
	s_nop 0
	v_addc_co_u32_e32 v161, vcc, 0, v171, vcc
	v_add_co_u32_e32 v172, vcc, s35, v170
	v_mfma_f32_16x16x32_bf16 v[92:95], v[120:123], v[148:151], v[92:95]
	s_nop 0
	v_addc_co_u32_e32 v173, vcc, 0, v171, vcc
	v_readlane_b32 s78, v253, 6
	v_mfma_f32_16x16x32_bf16 v[124:127], v[128:131], v[148:151], v[20:23]
	v_readlane_b32 s79, v253, 7
	v_readlane_b32 s80, v253, 8
	v_readlane_b32 s81, v253, 9
	v_mfma_f32_16x16x32_bf16 v[148:151], v[152:155], v[148:151], v[16:19]
	global_load_dwordx4 v[20:23], v[170:171], off
	s_nop 1
	global_load_dwordx4 v[16:19], v[160:161], off
	v_add_co_u32_e32 v170, vcc, s36, v170
	ds_read_b128 v[160:163], v178 offset:6912
	s_waitcnt lgkmcnt(1)
	v_mfma_f32_16x16x32_bf16 v[212:215], v[120:123], v[156:159], v[28:31]
	v_addc_co_u32_e32 v171, vcc, 0, v171, vcc
	v_readlane_b32 s82, v253, 10
	v_mfma_f32_16x16x32_bf16 v[216:219], v[128:131], v[156:159], v[24:27]
	global_load_dwordx4 v[28:31], v[172:173], off
	s_nop 1
	global_load_dwordx4 v[24:27], v[170:171], off
	ds_read_b128 v[220:223], v178 offset:9216
	v_readlane_b32 s83, v253, 11
	v_mfma_f32_16x16x32_bf16 v[88:91], v[116:119], v[156:159], v[88:91]
	s_mov_b64 s[60:61], s[88:89]
	s_mov_b64 s[62:63], s[90:91]
	ds_write_b64 v210, v[12:13]
	v_mfma_f32_16x16x32_bf16 v[84:87], v[152:155], v[156:159], v[84:87]
	ds_write_b64 v209, v[8:9]
	s_waitcnt lgkmcnt(3)
	v_mfma_f32_16x16x32_bf16 v[8:11], v[116:119], v[160:163], v[72:75]
	s_waitcnt vmcnt(9)
	v_cvt_pk_bf16_f32 v0, v0, v1
	v_cvt_pk_bf16_f32 v1, v2, v3
	v_mfma_f32_16x16x32_bf16 v[12:15], v[120:123], v[160:163], v[60:63]
	v_mfma_f32_16x16x32_bf16 v[60:63], v[128:131], v[160:163], v[68:71]
	v_mfma_f32_16x16x32_bf16 v[68:71], v[152:155], v[160:163], v[76:79]
	s_waitcnt lgkmcnt(2)
	v_mfma_f32_16x16x32_bf16 v[72:75], v[116:119], v[220:223], v[80:83]
	s_nop 0
	ds_read_b128 v[76:79], v178 offset:64
	s_nop 0
	ds_read_b128 v[80:83], v178 offset:2368
	ds_read_b128 v[116:119], v178 offset:4672
	ds_write_b64 v206, v[0:1]
	v_mfma_f32_16x16x32_bf16 v[64:67], v[120:123], v[220:223], v[64:67]
	v_cvt_pk_bf16_f32 v120, v4, v5
	v_cvt_pk_bf16_f32 v121, v6, v7
	ds_write_b64 v208, v[120:121]
	v_mfma_f32_16x16x32_bf16 v[4:7], v[128:131], v[220:223], v[56:59]
	v_mfma_f32_16x16x32_bf16 v[0:3], v[152:155], v[220:223], v[52:55]
	s_nop 2
	ds_read_b64_tr_b16 v[52:53], v205
	ds_read_b64_tr_b16 v[54:55], v207
	ds_read_b64_tr_b16 v[56:57], v203
	ds_read_b64_tr_b16 v[58:59], v204
	ds_read_b64_tr_b16 v[120:121], v200
	ds_read_b64_tr_b16 v[122:123], v201
	ds_read_b64_tr_b16 v[128:129], v198
	ds_read_b64_tr_b16 v[130:131], v199
	ds_read_b128 v[152:155], v178 offset:6976
	ds_read_b128 v[156:159], v178 offset:9280
	s_waitcnt lgkmcnt(8)
	v_mfma_f32_16x16x32_bf16 v[112:115], v[52:55], v[76:79], v[112:115]
	s_waitcnt vmcnt(8)
	ds_write_b128 v195, v[44:47] offset:46080
	s_waitcnt vmcnt(7)
	ds_write_b128 v195, v[36:39] offset:55296
	s_waitcnt lgkmcnt(8)
	v_mfma_f32_16x16x32_bf16 v[108:111], v[56:59], v[76:79], v[108:111]
	s_waitcnt lgkmcnt(6)
	v_mfma_f32_16x16x32_bf16 v[104:107], v[120:123], v[76:79], v[104:107]
	s_waitcnt lgkmcnt(4)
	v_mfma_f32_16x16x32_bf16 v[76:79], v[128:131], v[76:79], v[100:103]
	v_mfma_f32_16x16x32_bf16 v[96:99], v[52:55], v[80:83], v[96:99]
	v_mfma_f32_16x16x32_bf16 v[92:95], v[56:59], v[80:83], v[92:95]
	v_mfma_f32_16x16x32_bf16 v[100:103], v[120:123], v[80:83], v[124:127]
	v_mfma_f32_16x16x32_bf16 v[80:83], v[128:131], v[80:83], v[148:151]
	v_mfma_f32_16x16x32_bf16 v[88:91], v[52:55], v[116:119], v[88:91]
	v_mfma_f32_16x16x32_bf16 v[124:127], v[56:59], v[116:119], v[212:215]
	v_mfma_f32_16x16x32_bf16 v[148:151], v[120:123], v[116:119], v[216:219]
	v_mfma_f32_16x16x32_bf16 v[84:87], v[128:131], v[116:119], v[84:87]
	s_waitcnt lgkmcnt(3)
	v_mfma_f32_16x16x32_bf16 v[116:119], v[52:55], v[152:155], v[8:11]
	s_waitcnt vmcnt(6)
	ds_write_b128 v195, v[40:43] offset:64512
	s_waitcnt vmcnt(5)
	ds_write_b128 v196, v[32:35]
	s_waitcnt vmcnt(4)
	ds_write_b128 v197, v[48:51]
	v_add_u32_e32 v8, s51, v174
	ds_read_b32 v132, v202
	v_mfma_f32_16x16x32_bf16 v[160:163], v[56:59], v[152:155], v[12:15]
	s_waitcnt lgkmcnt(0)
	v_lshl_add_u64 v[10:11], v[132:133], 1, s[92:93]
	s_nop 0
	v_add_u32_e32 v14, 48, v8
	ds_read2st64_b32 v[8:9], v14 offset0:20 offset1:28
	ds_read2st64_b32 v[14:15], v14 offset0:36 offset1:44
	v_mfma_f32_16x16x32_bf16 v[56:59], v[56:59], v[156:159], v[64:67]
	s_waitcnt lgkmcnt(1)
	v_mov_b32_e32 v132, v8
	v_lshl_add_u64 v[12:13], v[132:133], 1, s[92:93]
	v_mov_b32_e32 v132, v9
	v_lshl_add_u64 v[8:9], v[132:133], 1, s[92:93]
	s_waitcnt lgkmcnt(0)
	v_mov_b32_e32 v132, v14
	global_load_dwordx4 v[36:39], v[10:11], off
	global_load_dwordx4 v[32:35], v[12:13], off
	v_lshl_add_u64 v[10:11], v[132:133], 1, s[92:93]
	v_mov_b32_e32 v132, v15
	v_mfma_f32_16x16x32_bf16 v[64:67], v[120:123], v[156:159], v[4:7]
	global_load_dwordx4 v[44:47], v[8:9], off
	global_load_dwordx4 v[40:43], v[10:11], off
	s_nop 0
	v_lshl_add_u64 v[4:5], v[132:133], 1, s[92:93]
	global_load_dwordx4 v[48:51], v[4:5], off
	v_mfma_f32_16x16x32_bf16 v[60:63], v[120:123], v[152:155], v[60:63]
	v_mfma_f32_16x16x32_bf16 v[68:71], v[128:131], v[152:155], v[68:71]
	v_mfma_f32_16x16x32_bf16 v[52:55], v[52:55], v[156:159], v[72:75]
	v_mfma_f32_16x16x32_bf16 v[72:75], v[128:131], v[156:159], v[0:3]
	s_barrier
	ds_read_b64_tr_b16 v[120:121], v193
	ds_read_b64_tr_b16 v[122:123], v194
	ds_read_b128 v[0:3], v178 offset:46080
	ds_read_b64_tr_b16 v[128:129], v190
	ds_read_b64_tr_b16 v[130:131], v191
	ds_read_b64_tr_b16 v[152:153], v192
	ds_read_b128 v[4:7], v178 offset:48384
	ds_read_b128 v[156:159], v178 offset:55296
	ds_read_b64_tr_b16 v[154:155], v189
	ds_read_b64_tr_b16 v[190:191], v187
	ds_read_b64_tr_b16 v[192:193], v188
	s_waitcnt lgkmcnt(8)
	v_mfma_f32_16x16x32_bf16 v[112:115], v[120:123], v[0:3], v[112:115]
	ds_read_b128 v[194:197], v178 offset:50688
	s_waitcnt lgkmcnt(7)
	v_mfma_f32_16x16x32_bf16 v[108:111], v[128:131], v[0:3], v[108:111]
	s_waitcnt lgkmcnt(3)
	v_mfma_f32_16x16x32_bf16 v[104:107], v[152:155], v[0:3], v[104:107]
	s_waitcnt lgkmcnt(1)
	v_mfma_f32_16x16x32_bf16 v[76:79], v[190:193], v[0:3], v[76:79]
	v_lshl_add_u64 v[0:1], v[164:165], 0, v[136:137]
	v_lshl_add_u64 v[0:1], v[0:1], 0, s[14:15]
	v_lshl_add_u64 v[0:1], v[0:1], 0, v[144:145]
	v_lshl_add_u64 v[0:1], v[0:1], 0, v[146:147]
	v_add_co_u32_e32 v2, vcc, s34, v0
	v_mfma_f32_16x16x32_bf16 v[96:99], v[120:123], v[4:7], v[96:99]
	s_nop 0
	v_addc_co_u32_e32 v3, vcc, 0, v1, vcc
	global_load_dwordx4 v[12:15], v[0:1], off
	global_load_dwordx4 v[8:11], v[2:3], off
	v_add_co_u32_e32 v2, vcc, s35, v0
	v_mfma_f32_16x16x32_bf16 v[92:95], v[128:131], v[4:7], v[92:95]
	s_nop 0
	v_addc_co_u32_e32 v3, vcc, 0, v1, vcc
	v_add_co_u32_e32 v0, vcc, s36, v0
	v_mfma_f32_16x16x32_bf16 v[100:103], v[152:155], v[4:7], v[100:103]
	s_nop 0
	v_addc_co_u32_e32 v1, vcc, 0, v1, vcc
	ds_read_b128 v[198:201], v178 offset:52992
	v_mfma_f32_16x16x32_bf16 v[80:83], v[190:193], v[4:7], v[80:83]
	global_load_dwordx4 v[4:7], v[2:3], off
	s_nop 0
	global_load_dwordx4 v[0:3], v[0:1], off
	s_waitcnt lgkmcnt(1)
	v_mfma_f32_16x16x32_bf16 v[88:91], v[120:123], v[194:197], v[88:91]
	v_mfma_f32_16x16x32_bf16 v[148:151], v[152:155], v[194:197], v[148:151]
	v_mfma_f32_16x16x32_bf16 v[202:205], v[128:131], v[194:197], v[124:127]
	v_mfma_f32_16x16x32_bf16 v[194:197], v[190:193], v[194:197], v[84:87]
	s_waitcnt lgkmcnt(0)
	v_mfma_f32_16x16x32_bf16 v[206:209], v[120:123], v[198:201], v[116:119]
	v_mfma_f32_16x16x32_bf16 v[160:163], v[128:131], v[198:201], v[160:163]
	v_mfma_f32_16x16x32_bf16 v[60:63], v[152:155], v[198:201], v[60:63]
	v_mfma_f32_16x16x32_bf16 v[68:71], v[190:193], v[198:201], v[68:71]
	v_mfma_f32_16x16x32_bf16 v[152:155], v[152:155], v[156:159], v[64:67]
	s_nop 2
	ds_read_b128 v[64:67], v178 offset:46144
	ds_read_b128 v[84:87], v178 offset:48448
	ds_read_b128 v[198:201], v178 offset:50752
	v_mfma_f32_16x16x32_bf16 v[52:55], v[120:123], v[156:159], v[52:55]
	v_mfma_f32_16x16x32_bf16 v[56:59], v[128:131], v[156:159], v[56:59]
	v_mfma_f32_16x16x32_bf16 v[156:159], v[190:193], v[156:159], v[72:75]
	ds_read_b64_tr_b16 v[188:189], v185
	ds_read_b64_tr_b16 v[190:191], v186
	ds_read_b64_tr_b16 v[210:211], v183
	ds_read_b64_tr_b16 v[212:213], v184
	ds_read_b64_tr_b16 v[184:185], v181
	ds_read_b64_tr_b16 v[186:187], v182
	ds_read_b64_tr_b16 v[214:215], v179
	ds_read_b64_tr_b16 v[216:217], v180
	s_waitcnt lgkmcnt(6)
	v_mfma_f32_16x16x32_bf16 v[124:127], v[188:191], v[64:67], v[112:115]
	s_waitcnt lgkmcnt(4)
	v_mfma_f32_16x16x32_bf16 v[116:119], v[210:213], v[64:67], v[108:111]
	s_waitcnt lgkmcnt(2)
	v_mfma_f32_16x16x32_bf16 v[128:131], v[184:187], v[64:67], v[104:107]
	s_waitcnt lgkmcnt(0)
	v_mfma_f32_16x16x32_bf16 v[120:123], v[214:217], v[64:67], v[76:79]
	v_mfma_f32_16x16x32_bf16 v[104:107], v[210:213], v[84:87], v[92:95]
	v_mfma_f32_16x16x32_bf16 v[92:95], v[184:187], v[198:201], v[148:151]
	ds_read_b128 v[64:67], v178 offset:53056
	s_nop 1
	ds_read_b128 v[148:151], v178 offset:55360
	v_mfma_f32_16x16x32_bf16 v[112:115], v[188:191], v[84:87], v[96:99]
	v_mfma_f32_16x16x32_bf16 v[108:111], v[184:187], v[84:87], v[100:103]
	v_mfma_f32_16x16x32_bf16 v[100:103], v[214:217], v[84:87], v[80:83]
	v_mfma_f32_16x16x32_bf16 v[96:99], v[188:191], v[198:201], v[88:91]
	v_mfma_f32_16x16x32_bf16 v[84:87], v[210:213], v[198:201], v[202:205]
	v_mfma_f32_16x16x32_bf16 v[88:91], v[214:217], v[198:201], v[194:197]
	s_waitcnt lgkmcnt(1)
	v_mfma_f32_16x16x32_bf16 v[80:83], v[188:191], v[64:67], v[206:209]
	v_mfma_f32_16x16x32_bf16 v[72:75], v[210:213], v[64:67], v[160:163]
	v_mfma_f32_16x16x32_bf16 v[76:79], v[184:187], v[64:67], v[60:63]
	v_mfma_f32_16x16x32_bf16 v[68:71], v[214:217], v[64:67], v[68:71]
	s_waitcnt lgkmcnt(0)
	v_mfma_f32_16x16x32_bf16 v[64:67], v[188:191], v[148:151], v[52:55]
	v_mfma_f32_16x16x32_bf16 v[56:59], v[210:213], v[148:151], v[56:59]
	v_mfma_f32_16x16x32_bf16 v[60:63], v[184:187], v[148:151], v[152:155]
	v_mfma_f32_16x16x32_bf16 v[52:55], v[214:217], v[148:151], v[156:159]
	v_add_u32_e32 v145, s25, v169
	v_cmp_lt_i32_e32 vcc, v145, v166
	v_lshlrev_b32_e32 v132, 1, v138
	v_lshlrev_b32_e32 v148, 1, v140
	v_mbcnt_lo_u32_b32 v228, -1, 0
	v_mbcnt_hi_u32_b32 v228, -1, v228
	v_bfe_u32 v228, v228, 4, 1
	v_mul_u32_u24_e32 v228, 24, v228
	v_add_u32_e32 v148, v148, v228
	s_and_saveexec_b64 s[14:15], vcc
	s_cbranch_execz .LBB0_2373
	v_mul_f32_e32 v147, 0xbfb8aa3b, v124
	v_exp_f32_e32 v147, v147
	v_mul_f32_e32 v149, 0xbfb8aa3b, v125
	v_exp_f32_e32 v149, v149
	v_mul_f32_e32 v151, 0xbfb8aa3b, v127
	v_add_f32_e32 v147, 1.0, v147
	v_rcp_f32_e32 v150, v147
	v_mul_f32_e32 v147, 0xbfb8aa3b, v126
	v_exp_f32_e32 v147, v147
	v_exp_f32_e32 v153, v151
	v_add_f32_e32 v149, 1.0, v149
	v_rcp_f32_e32 v151, v149
	v_add_f32_e32 v147, 1.0, v147
	v_rcp_f32_e32 v152, v147
	v_add_f32_e32 v147, 1.0, v153
	v_rcp_f32_e32 v153, v147
	v_pk_mul_f32 v[124:125], v[124:125], v[150:151]
	v_readlane_b32 s16, v254, 1
	v_pk_mul_f32 v[124:125], v[128:129], v[124:125]
	v_pk_mul_f32 v[126:127], v[126:127], v[152:153]
	v_cvt_pk_bf16_f32 v124, v124, v125
	v_mul_f32_e32 v125, 0xbfb8aa3b, v116
	v_pk_mul_f32 v[126:127], v[130:131], v[126:127]
	v_exp_f32_e32 v130, v125
	v_mul_f32_e32 v125, 0xbfb8aa3b, v117
	v_exp_f32_e32 v131, v125
	v_cvt_pk_bf16_f32 v125, v126, v127
	v_add_f32_e32 v126, 1.0, v130
	v_mul_f32_e32 v130, 0xbfb8aa3b, v118
	v_add_f32_e32 v127, 1.0, v131
	v_mul_f32_e32 v131, 0xbfb8aa3b, v119
	v_exp_f32_e32 v130, v130
	v_exp_f32_e32 v131, v131
	v_add_u32_e32 v128, v139, v145
	v_rcp_f32_e32 v126, v126
	v_add_f32_e32 v130, 1.0, v130
	v_add_f32_e32 v131, 1.0, v131
	v_rcp_f32_e32 v127, v127
	v_rcp_f32_e32 v130, v130
	v_rcp_f32_e32 v131, v131
	v_ashrrev_i32_e32 v129, 31, v128
	v_lshlrev_b64 v[128:129], 9, v[128:129]
	v_readlane_b32 s17, v254, 2
	v_pk_mul_f32 v[116:117], v[116:117], v[126:127]
	v_pk_mul_f32 v[118:119], v[118:119], v[130:131]
	v_lshl_add_u64 v[128:129], s[16:17], 0, v[128:129]
	v_lshl_add_u64 v[128:129], s[12:13], 1, v[128:129]
	v_lshl_add_u64 v[128:129], v[128:129], 0, v[132:133]
	v_mov_b32_e32 v149, v133
	v_pk_mul_f32 v[116:117], v[120:121], v[116:117]
	v_pk_mul_f32 v[118:119], v[122:123], v[118:119]
	v_lshl_add_u64 v[128:129], v[128:129], 0, v[148:149]
	v_cvt_pk_bf16_f32 v116, v116, v117
	v_cvt_pk_bf16_f32 v117, v118, v119
	v_mov_b32_e32 v224, v124
	v_mov_b32_e32 v225, v125
	v_mov_b32_e32 v226, v116
	v_mov_b32_e32 v227, v117
	s_nop 1
	v_permlane16_swap_b32 v224, v226
	v_permlane16_swap_b32 v225, v227
	global_store_dwordx4 v[128:129], v[224:227], off
.LBB0_2373:
	s_or_b64 exec, exec, s[14:15]
	v_add_u32_e32 v116, s25, v252
	v_cmp_lt_i32_e32 vcc, v116, v166
	s_and_saveexec_b64 s[14:15], vcc
	s_cbranch_execz .LBB0_2375
	v_mul_f32_e32 v117, 0xbfb8aa3b, v112
	v_exp_f32_e32 v117, v117
	v_mul_f32_e32 v118, 0xbfb8aa3b, v113
	v_exp_f32_e32 v118, v118
	v_mul_f32_e32 v120, 0xbfb8aa3b, v115
	v_add_f32_e32 v117, 1.0, v117
	v_exp_f32_e32 v121, v120
	v_add_f32_e32 v119, 1.0, v118
	v_rcp_f32_e32 v118, v117
	v_mul_f32_e32 v117, 0xbfb8aa3b, v114
	v_exp_f32_e32 v117, v117
	v_rcp_f32_e32 v119, v119
	v_readlane_b32 s16, v254, 1
	v_readlane_b32 s17, v254, 2
	v_add_f32_e32 v117, 1.0, v117
	v_rcp_f32_e32 v120, v117
	v_add_f32_e32 v117, 1.0, v121
	v_rcp_f32_e32 v121, v117
	v_pk_mul_f32 v[112:113], v[112:113], v[118:119]
	v_mov_b32_e32 v149, v133
	v_pk_mul_f32 v[108:109], v[108:109], v[112:113]
	v_pk_mul_f32 v[112:113], v[114:115], v[120:121]
	v_cvt_pk_bf16_f32 v108, v108, v109
	v_mul_f32_e32 v109, 0xbfb8aa3b, v104
	v_exp_f32_e32 v114, v109
	v_mul_f32_e32 v109, 0xbfb8aa3b, v105
	v_exp_f32_e32 v115, v109
	v_pk_mul_f32 v[110:111], v[110:111], v[112:113]
	v_add_u32_e32 v112, v139, v116
	v_cvt_pk_bf16_f32 v109, v110, v111
	v_add_f32_e32 v110, 1.0, v114
	v_add_f32_e32 v111, 1.0, v115
	v_mul_f32_e32 v114, 0xbfb8aa3b, v106
	v_mul_f32_e32 v115, 0xbfb8aa3b, v107
	v_exp_f32_e32 v114, v114
	v_exp_f32_e32 v115, v115
	v_rcp_f32_e32 v110, v110
	v_rcp_f32_e32 v111, v111
	v_add_f32_e32 v114, 1.0, v114
	v_add_f32_e32 v115, 1.0, v115
	v_rcp_f32_e32 v114, v114
	v_rcp_f32_e32 v115, v115
	v_ashrrev_i32_e32 v113, 31, v112
	v_lshlrev_b64 v[112:113], 9, v[112:113]
	v_lshl_add_u64 v[112:113], s[16:17], 0, v[112:113]
	v_pk_mul_f32 v[104:105], v[104:105], v[110:111]
	v_lshl_add_u64 v[112:113], s[12:13], 1, v[112:113]
	v_pk_mul_f32 v[100:101], v[100:101], v[104:105]
	v_pk_mul_f32 v[104:105], v[106:107], v[114:115]
	v_lshl_add_u64 v[112:113], v[112:113], 0, v[132:133]
	v_pk_mul_f32 v[102:103], v[102:103], v[104:105]
	v_lshl_add_u64 v[112:113], v[112:113], 0, v[148:149]
	v_cvt_pk_bf16_f32 v100, v100, v101
	v_cvt_pk_bf16_f32 v101, v102, v103
	v_mov_b32_e32 v224, v108
	v_mov_b32_e32 v225, v109
	v_mov_b32_e32 v226, v100
	v_mov_b32_e32 v227, v101
	s_nop 1
	v_permlane16_swap_b32 v224, v226
	v_permlane16_swap_b32 v225, v227
	global_store_dwordx4 v[112:113], v[224:227], off
.LBB0_2375:
	s_or_b64 exec, exec, s[14:15]
	v_add_u32_e32 v100, 32, v169
	v_add_u32_e32 v100, s25, v100
	v_cmp_lt_i32_e32 vcc, v100, v166
	s_and_saveexec_b64 s[14:15], vcc
	s_cbranch_execz .LBB0_2377
	v_mul_f32_e32 v101, 0xbfb8aa3b, v96
	v_exp_f32_e32 v101, v101
	v_mul_f32_e32 v102, 0xbfb8aa3b, v97
	v_exp_f32_e32 v102, v102
	v_mul_f32_e32 v104, 0xbfb8aa3b, v99
	v_add_f32_e32 v101, 1.0, v101
	v_exp_f32_e32 v105, v104
	v_add_f32_e32 v103, 1.0, v102
	v_rcp_f32_e32 v102, v101
	v_mul_f32_e32 v101, 0xbfb8aa3b, v98
	v_exp_f32_e32 v101, v101
	v_rcp_f32_e32 v103, v103
	v_readlane_b32 s16, v254, 1
	v_readlane_b32 s17, v254, 2
	v_add_f32_e32 v101, 1.0, v101
	v_rcp_f32_e32 v104, v101
	v_add_f32_e32 v101, 1.0, v105
	v_rcp_f32_e32 v105, v101
	v_pk_mul_f32 v[96:97], v[96:97], v[102:103]
	v_mov_b32_e32 v149, v133
	v_pk_mul_f32 v[92:93], v[92:93], v[96:97]
	v_pk_mul_f32 v[96:97], v[98:99], v[104:105]
	v_cvt_pk_bf16_f32 v92, v92, v93
	v_mul_f32_e32 v93, 0xbfb8aa3b, v84
	v_exp_f32_e32 v98, v93
	v_mul_f32_e32 v93, 0xbfb8aa3b, v85
	v_exp_f32_e32 v99, v93
	v_pk_mul_f32 v[94:95], v[94:95], v[96:97]
	v_add_u32_e32 v96, v139, v100
	v_cvt_pk_bf16_f32 v93, v94, v95
	v_add_f32_e32 v94, 1.0, v98
	v_add_f32_e32 v95, 1.0, v99
	v_mul_f32_e32 v98, 0xbfb8aa3b, v86
	v_mul_f32_e32 v99, 0xbfb8aa3b, v87
	v_exp_f32_e32 v98, v98
	v_exp_f32_e32 v99, v99
	v_rcp_f32_e32 v94, v94
	v_rcp_f32_e32 v95, v95
	v_add_f32_e32 v98, 1.0, v98
	v_add_f32_e32 v99, 1.0, v99
	v_rcp_f32_e32 v98, v98
	v_rcp_f32_e32 v99, v99
	v_ashrrev_i32_e32 v97, 31, v96
	v_lshlrev_b64 v[96:97], 9, v[96:97]
	v_lshl_add_u64 v[96:97], s[16:17], 0, v[96:97]
	v_lshl_add_u64 v[96:97], s[12:13], 1, v[96:97]
	v_pk_mul_f32 v[84:85], v[84:85], v[94:95]
	v_pk_mul_f32 v[86:87], v[86:87], v[98:99]
	v_lshl_add_u64 v[96:97], v[96:97], 0, v[132:133]
	v_pk_mul_f32 v[84:85], v[88:89], v[84:85]
	v_pk_mul_f32 v[86:87], v[90:91], v[86:87]
	v_lshl_add_u64 v[96:97], v[96:97], 0, v[148:149]
	v_cvt_pk_bf16_f32 v84, v84, v85
	v_cvt_pk_bf16_f32 v85, v86, v87
	v_mov_b32_e32 v224, v92
	v_mov_b32_e32 v225, v93
	v_mov_b32_e32 v226, v84
	v_mov_b32_e32 v227, v85
	s_nop 1
	v_permlane16_swap_b32 v224, v226
	v_permlane16_swap_b32 v225, v227
	global_store_dwordx4 v[96:97], v[224:227], off
.LBB0_2377:
	s_or_b64 exec, exec, s[14:15]
	v_add_u32_e32 v84, 48, v169
	v_add_u32_e32 v84, s25, v84
	v_cmp_lt_i32_e32 vcc, v84, v166
	s_and_saveexec_b64 s[14:15], vcc
	s_cbranch_execz .LBB0_2379
	v_mul_f32_e32 v85, 0xbfb8aa3b, v80
	v_exp_f32_e32 v85, v85
	v_mul_f32_e32 v86, 0xbfb8aa3b, v81
	v_exp_f32_e32 v86, v86
	v_mul_f32_e32 v88, 0xbfb8aa3b, v83
	v_add_f32_e32 v85, 1.0, v85
	v_exp_f32_e32 v89, v88
	v_add_f32_e32 v87, 1.0, v86
	v_rcp_f32_e32 v86, v85
	v_mul_f32_e32 v85, 0xbfb8aa3b, v82
	v_exp_f32_e32 v85, v85
	v_rcp_f32_e32 v87, v87
	v_readlane_b32 s16, v254, 1
	v_readlane_b32 s17, v254, 2
	v_add_f32_e32 v85, 1.0, v85
	v_rcp_f32_e32 v88, v85
	v_add_f32_e32 v85, 1.0, v89
	v_rcp_f32_e32 v89, v85
	v_pk_mul_f32 v[80:81], v[80:81], v[86:87]
	v_mov_b32_e32 v149, v133
	v_pk_mul_f32 v[76:77], v[76:77], v[80:81]
	v_pk_mul_f32 v[80:81], v[82:83], v[88:89]
	v_cvt_pk_bf16_f32 v76, v76, v77
	v_mul_f32_e32 v77, 0xbfb8aa3b, v72
	v_exp_f32_e32 v82, v77
	v_mul_f32_e32 v77, 0xbfb8aa3b, v73
	v_exp_f32_e32 v83, v77
	v_pk_mul_f32 v[78:79], v[78:79], v[80:81]
	v_add_u32_e32 v80, v139, v84
	v_cvt_pk_bf16_f32 v77, v78, v79
	v_add_f32_e32 v78, 1.0, v82
	v_add_f32_e32 v79, 1.0, v83
	v_mul_f32_e32 v82, 0xbfb8aa3b, v74
	v_mul_f32_e32 v83, 0xbfb8aa3b, v75
	v_exp_f32_e32 v82, v82
	v_exp_f32_e32 v83, v83
	v_rcp_f32_e32 v78, v78
	v_rcp_f32_e32 v79, v79
	v_add_f32_e32 v82, 1.0, v82
	v_add_f32_e32 v83, 1.0, v83
	v_rcp_f32_e32 v82, v82
	v_rcp_f32_e32 v83, v83
	v_ashrrev_i32_e32 v81, 31, v80
	v_lshlrev_b64 v[80:81], 9, v[80:81]
	v_lshl_add_u64 v[80:81], s[16:17], 0, v[80:81]
	v_pk_mul_f32 v[72:73], v[72:73], v[78:79]
	v_lshl_add_u64 v[80:81], s[12:13], 1, v[80:81]
	v_pk_mul_f32 v[68:69], v[68:69], v[72:73]
	v_pk_mul_f32 v[72:73], v[74:75], v[82:83]
	v_lshl_add_u64 v[80:81], v[80:81], 0, v[132:133]
	v_pk_mul_f32 v[70:71], v[70:71], v[72:73]
	v_lshl_add_u64 v[80:81], v[80:81], 0, v[148:149]
	v_cvt_pk_bf16_f32 v68, v68, v69
	v_cvt_pk_bf16_f32 v69, v70, v71
	v_mov_b32_e32 v224, v76
	v_mov_b32_e32 v225, v77
	v_mov_b32_e32 v226, v68
	v_mov_b32_e32 v227, v69
	s_nop 1
	v_permlane16_swap_b32 v224, v226
	v_permlane16_swap_b32 v225, v227
	global_store_dwordx4 v[80:81], v[224:227], off

.LBB0_2381:
	v_mul_f32_e32 v69, 0xbfb8aa3b, v64
	v_exp_f32_e32 v69, v69
	v_mul_f32_e32 v70, 0xbfb8aa3b, v65
	v_exp_f32_e32 v70, v70
	v_mul_f32_e32 v72, 0xbfb8aa3b, v67
	v_add_f32_e32 v69, 1.0, v69
	v_exp_f32_e32 v73, v72
	v_add_f32_e32 v71, 1.0, v70
	v_rcp_f32_e32 v70, v69
	v_mul_f32_e32 v69, 0xbfb8aa3b, v66
	v_exp_f32_e32 v69, v69
	v_rcp_f32_e32 v71, v71
	v_readlane_b32 s16, v254, 1
	v_readlane_b32 s17, v254, 2
	v_add_f32_e32 v69, 1.0, v69
	v_rcp_f32_e32 v72, v69
	v_add_f32_e32 v69, 1.0, v73
	v_rcp_f32_e32 v73, v69
	v_pk_mul_f32 v[64:65], v[64:65], v[70:71]
	v_mov_b32_e32 v149, v133
	v_pk_mul_f32 v[60:61], v[60:61], v[64:65]
	v_pk_mul_f32 v[64:65], v[66:67], v[72:73]
	v_cvt_pk_bf16_f32 v60, v60, v61
	v_mul_f32_e32 v61, 0xbfb8aa3b, v56
	v_exp_f32_e32 v66, v61
	v_mul_f32_e32 v61, 0xbfb8aa3b, v57
	v_exp_f32_e32 v67, v61
	v_pk_mul_f32 v[62:63], v[62:63], v[64:65]
	v_add_u32_e32 v64, v139, v68
	v_cvt_pk_bf16_f32 v61, v62, v63
	v_add_f32_e32 v62, 1.0, v66
	v_add_f32_e32 v63, 1.0, v67
	v_mul_f32_e32 v66, 0xbfb8aa3b, v58
	v_mul_f32_e32 v67, 0xbfb8aa3b, v59
	v_exp_f32_e32 v66, v66
	v_exp_f32_e32 v67, v67
	v_rcp_f32_e32 v62, v62
	v_rcp_f32_e32 v63, v63
	v_add_f32_e32 v66, 1.0, v66
	v_add_f32_e32 v67, 1.0, v67
	v_rcp_f32_e32 v66, v66
	v_rcp_f32_e32 v67, v67
	v_ashrrev_i32_e32 v65, 31, v64
	v_lshlrev_b64 v[64:65], 9, v[64:65]
	v_lshl_add_u64 v[64:65], s[16:17], 0, v[64:65]
	v_pk_mul_f32 v[56:57], v[56:57], v[62:63]
	v_lshl_add_u64 v[64:65], s[12:13], 1, v[64:65]
	v_pk_mul_f32 v[52:53], v[52:53], v[56:57]
	v_pk_mul_f32 v[56:57], v[58:59], v[66:67]
	v_lshl_add_u64 v[64:65], v[64:65], 0, v[132:133]
	v_pk_mul_f32 v[54:55], v[54:55], v[56:57]
	v_lshl_add_u64 v[64:65], v[64:65], 0, v[148:149]
	v_cvt_pk_bf16_f32 v52, v52, v53
	v_cvt_pk_bf16_f32 v53, v54, v55
	v_mov_b32_e32 v224, v60
	v_mov_b32_e32 v225, v61
	v_mov_b32_e32 v226, v52
	v_mov_b32_e32 v227, v53
	s_nop 1
	v_permlane16_swap_b32 v224, v226
	v_permlane16_swap_b32 v225, v227
	global_store_dwordx4 v[64:65], v[224:227], off
	s_or_b64 exec, exec, s[14:15]
	v_cmp_ne_u32_e32 vcc, 1, v177
	s_cbranch_vccnz .LBB0_2356
